# plus2
# baseline (speedup 1.0000x reference)
_Z6k_rec2PKiS0_S0_PK15HIP_vector_typeIjLj4EEPKfS6_PS2_PS1_IjLj2EEPf:
	v_readfirstlane_b32 s90, v0
	s_lshr_b32 s90, s90, 8
	s_load_dwordx2 s[6:7], s[0:1], 0x0
	s_load_dwordx2 s[4:5], s[0:1], 0x28
	s_load_dwordx4 s[72:75], s[0:1], 0x8
	v_cmp_gt_u32_e32 vcc, 32, v0
	s_and_saveexec_b64 s[8:9], vcc
	v_mov_b32_e32 v1, 0x22000
	v_lshl_or_b32 v1, v0, 2, v1
	v_mov_b32_e32 v2, 0
	ds_write_b32 v1, v2
	s_or_b64 exec, exec, s[8:9]
	v_mov_b32_e32 v3, 0
	v_lshlrev_b32_e32 v2, 2, v0
	s_waitcnt lgkmcnt(0)
	v_lshrrev_b32_e32 v214, 1, v0
	v_and_b32_e32 v214, 0xe0, v214
	global_load_dwordx4 v[216:219], v214, s[74:75]
	global_load_dwordx4 v[220:223], v214, s[72:73]
	global_load_dwordx3 v[224:226], v214, s[74:75] offset:16
	global_load_dwordx3 v[198:200], v214, s[72:73] offset:16
	global_load_dword v227, v214, s[74:75] offset:28
	global_load_dword v228, v214, s[72:73] offset:28
	v_lshl_add_u64 v[4:5], s[6:7], 0, v[2:3]
	s_movk_i32 s3, 0x1000
	v_or_b32_e32 v1, 0x400, v0
	v_add_co_u32_e32 v6, vcc, s3, v4
	v_lshlrev_b32_e32 v3, 2, v1
	s_nop 0
	v_addc_co_u32_e32 v7, vcc, 0, v5, vcc
	global_load_dword v68, v2, s[6:7]
	global_load_dword v69, v2, s[6:7] offset:2048
	global_load_dword v70, v3, s[6:7]
	global_load_dword v71, v[6:7], off offset:2048
	v_or_b32_e32 v165, 0x800, v0
	s_movk_i32 s3, 0x2000
	v_lshlrev_b32_e32 v6, 2, v165
	v_add_co_u32_e32 v2, vcc, s3, v4
	v_or_b32_e32 v232, 0xc00, v0
	s_nop 0
	v_addc_co_u32_e32 v3, vcc, 0, v5, vcc
	global_load_dword v72, v6, s[6:7]
	global_load_dword v73, v[2:3], off offset:2048
	v_lshlrev_b32_e32 v2, 2, v232
	global_load_dword v74, v2, s[6:7]
	s_movk_i32 s3, 0x3000
	v_add_co_u32_e32 v2, vcc, s3, v4
	s_ashr_i32 s3, s2, 31
	s_nop 0
	v_addc_co_u32_e32 v3, vcc, 0, v5, vcc
	global_load_dword v75, v[2:3], off offset:2048
	s_lshl_b64 s[6:7], s[2:3], 17
	s_add_u32 s4, s4, s6
	s_addc_u32 s5, s5, s7
	v_mbcnt_lo_u32_b32 v77, -1, 0
	v_mbcnt_hi_u32_b32 v77, -1, v77
	v_and_b32_e32 v83, 64, v77
	v_xor_b32_e32 v84, 32, v77
	v_add_u32_e32 v83, 64, v83
	v_cmp_lt_i32_e32 vcc, v84, v83
	v_xor_b32_e32 v85, 16, v77
	v_xor_b32_e32 v86, 8, v77
	v_cndmask_b32_e32 v84, v77, v84, vcc
	v_lshlrev_b32_e32 v234, 2, v84
	v_cmp_lt_i32_e32 vcc, v85, v83
	v_xor_b32_e32 v87, 4, v77
	v_xor_b32_e32 v88, 2, v77
	v_cndmask_b32_e32 v85, v77, v85, vcc
	v_lshlrev_b32_e32 v235, 2, v85
	v_cmp_lt_i32_e32 vcc, v86, v83
	v_xor_b32_e32 v89, 1, v77
	v_mov_b32_e32 v76, 0x20000
	v_cndmask_b32_e32 v86, v77, v86, vcc
	v_lshlrev_b32_e32 v236, 2, v86
	v_cmp_lt_i32_e32 vcc, v87, v83
	v_lshl_or_b32 v79, v1, 1, v76
	v_lshl_or_b32 v81, v165, 1, v76
	v_cndmask_b32_e32 v87, v77, v87, vcc
	v_cmp_lt_i32_e32 vcc, v88, v83
	v_lshlrev_b32_e32 v237, 2, v87
	v_lshl_or_b32 v76, v232, 1, v76
	v_cndmask_b32_e32 v88, v77, v88, vcc
	v_cmp_lt_i32_e32 vcc, v89, v83
	v_lshlrev_b32_e32 v238, 2, v88
	s_mov_b32 s3, 0
	v_cndmask_b32_e32 v77, v77, v89, vcc
	v_lshlrev_b32_e32 v239, 2, v77
	s_waitcnt vmcnt(7)
	v_lshlrev_b32_e32 v2, 1, v68
	s_waitcnt vmcnt(6)
	v_lshlrev_b32_e32 v4, 1, v69
	v_ashrrev_i32_e32 v3, 31, v2
	v_ashrrev_i32_e32 v5, 31, v4
	v_lshl_add_u64 v[10:11], v[2:3], 4, s[4:5]
	v_lshl_add_u64 v[20:21], v[4:5], 4, s[4:5]
	global_load_dwordx4 v[2:5], v[10:11], off offset:16
	global_load_dwordx4 v[6:9], v[10:11], off
	s_nop 0
	global_load_dwordx4 v[10:13], v[20:21], off offset:16
	global_load_dwordx4 v[14:17], v[20:21], off
	s_waitcnt vmcnt(9)
	v_lshlrev_b32_e32 v18, 1, v70
	v_ashrrev_i32_e32 v19, 31, v18
	v_lshl_add_u64 v[28:29], v[18:19], 4, s[4:5]
	global_load_dwordx4 v[18:21], v[28:29], off offset:16
	global_load_dwordx4 v[22:25], v[28:29], off
	s_waitcnt vmcnt(10)
	v_lshlrev_b32_e32 v26, 1, v71
	v_ashrrev_i32_e32 v27, 31, v26
	v_lshl_add_u64 v[36:37], v[26:27], 4, s[4:5]
	global_load_dwordx4 v[26:29], v[36:37], off offset:16
	global_load_dwordx4 v[30:33], v[36:37], off
	s_waitcnt vmcnt(11)
	v_lshlrev_b32_e32 v34, 1, v72
	v_ashrrev_i32_e32 v35, 31, v34
	v_lshl_add_u64 v[44:45], v[34:35], 4, s[4:5]
	global_load_dwordx4 v[34:37], v[44:45], off offset:16
	global_load_dwordx4 v[38:41], v[44:45], off
	s_waitcnt vmcnt(12)
	v_lshlrev_b32_e32 v42, 1, v73
	v_ashrrev_i32_e32 v43, 31, v42
	v_lshl_add_u64 v[52:53], v[42:43], 4, s[4:5]
	global_load_dwordx4 v[42:45], v[52:53], off offset:16
	global_load_dwordx4 v[46:49], v[52:53], off
	s_waitcnt vmcnt(13)
	v_lshlrev_b32_e32 v50, 1, v74
	v_ashrrev_i32_e32 v51, 31, v50
	v_lshl_add_u64 v[58:59], v[50:51], 4, s[4:5]
	global_load_dwordx4 v[50:53], v[58:59], off offset:16
	global_load_dwordx4 v[54:57], v[58:59], off
	s_waitcnt vmcnt(14)
	v_lshlrev_b32_e32 v58, 1, v75
	v_ashrrev_i32_e32 v59, 31, v58
	v_lshl_add_u64 v[66:67], v[58:59], 4, s[4:5]
	global_load_dwordx4 v[62:65], v[66:67], off
	global_load_dwordx4 v[58:61], v[66:67], off offset:16
	v_lshlrev_b32_e32 v67, 1, v0
	v_or_b32_e32 v233, 0x20000, v67
	s_load_dwordx4 s[8:11], s[0:1], 0x8
	s_load_dwordx2 s[14:15], s[0:1], 0x18
	s_load_dwordx2 s[12:13], s[0:1], 0x40
	s_load_dwordx2 s[6:7], s[0:1], 0x30
	v_or_b32_e32 v78, 0x20400, v67
	v_or_b32_e32 v80, 0x20c00, v67
	ds_write_b16 v233, v68
	ds_write_b16 v78, v69
	ds_write_b16 v79, v70
	ds_write_b16 v80, v71
	v_or_b32_e32 v82, 0x21400, v67
	v_or_b32_e32 v67, 0x21c00, v67
	ds_write_b16 v81, v72
	ds_write_b16 v82, v73
	ds_write_b16 v76, v74
	ds_write_b16 v67, v75
	v_mov_b32_e32 v246, v68
	v_mov_b32_e32 v247, v69
	v_mov_b32_e32 v248, v70
	v_mov_b32_e32 v249, v71
	v_mov_b32_e32 v250, v72
	v_mov_b32_e32 v251, v73
	v_mov_b32_e32 v252, v74
	v_mov_b32_e32 v253, v75
	v_and_b32_e32 v66, 63, v0
	v_cmp_eq_u32_e64 s[4:5], 0, v66
	s_waitcnt lgkmcnt(0)
	s_barrier
	s_waitcnt vmcnt(14)
	v_max3_f32 v84, |v6|, 0, |v7|
	v_max3_f32 v84, v84, |v8|, |v9|
	v_max3_f32 v84, v84, |v2|, |v3|
	v_max3_f32 v84, v84, |v4|, |v5|
	s_waitcnt vmcnt(12)
	v_max3_f32 v84, v84, |v14|, |v15|
	v_max3_f32 v84, v84, |v16|, |v17|
	v_max3_f32 v84, v84, |v10|, |v11|
	v_max3_f32 v84, v84, |v12|, |v13|
	s_waitcnt vmcnt(10)
	v_max3_f32 v84, v84, |v22|, |v23|
	v_max3_f32 v84, v84, |v24|, |v25|
	v_max3_f32 v84, v84, |v18|, |v19|
	v_max3_f32 v84, v84, |v20|, |v21|
	s_waitcnt vmcnt(8)
	v_max3_f32 v84, v84, |v30|, |v31|
	v_max3_f32 v84, v84, |v32|, |v33|
	v_max3_f32 v84, v84, |v26|, |v27|
	v_max3_f32 v84, v84, |v28|, |v29|
	s_waitcnt vmcnt(6)
	v_max3_f32 v84, v84, |v38|, |v39|
	v_max3_f32 v84, v84, |v40|, |v41|
	v_max3_f32 v84, v84, |v34|, |v35|
	v_max3_f32 v84, v84, |v36|, |v37|
	s_waitcnt vmcnt(4)
	v_max3_f32 v84, v84, |v46|, |v47|
	v_max3_f32 v84, v84, |v48|, |v49|
	v_max3_f32 v84, v84, |v42|, |v43|
	v_max3_f32 v84, v84, |v44|, |v45|
	s_waitcnt vmcnt(2)
	v_max3_f32 v84, v84, |v54|, |v55|
	v_max3_f32 v84, v84, |v56|, |v57|
	v_max3_f32 v84, v84, |v50|, |v51|
	v_max3_f32 v84, v84, |v52|, |v53|
	s_waitcnt vmcnt(1)
	v_max3_f32 v84, v84, |v62|, |v63|
	v_max3_f32 v84, v84, |v64|, |v65|
	s_waitcnt vmcnt(0)
	v_max3_f32 v84, v84, |v58|, |v59|
	v_max3_f32 v84, v84, |v60|, |v61|
	ds_bpermute_b32 v90, v234, v84
	s_waitcnt lgkmcnt(0)
	v_max_f32_e32 v85, v90, v90
	v_max_f32_e32 v84, v84, v85
	ds_bpermute_b32 v85, v235, v84
	s_waitcnt lgkmcnt(0)
	v_max_f32_e32 v85, v85, v85
	v_max_f32_e32 v84, v84, v85
	ds_bpermute_b32 v85, v236, v84
	s_waitcnt lgkmcnt(0)
	v_max_f32_e32 v83, v85, v85
	v_max_f32_e32 v83, v84, v83
	ds_bpermute_b32 v84, v237, v83
	s_waitcnt lgkmcnt(0)
	v_max_f32_e32 v68, v84, v84
	v_max_f32_e32 v68, v83, v68
	ds_bpermute_b32 v69, v238, v68
	s_waitcnt lgkmcnt(0)
	v_max_f32_e32 v67, v69, v69
	v_max_f32_e32 v67, v68, v67
	ds_bpermute_b32 v68, v239, v67
	s_and_saveexec_b64 s[16:17], s[4:5]
	s_cbranch_execz .LBB3_7
	s_waitcnt lgkmcnt(0)
	v_max_f32_e32 v68, v68, v68
	v_max_f32_e32 v67, v67, v67
	s_mov_b64 s[18:19], exec
	v_max_f32_e32 v67, v67, v68
